# baseline (speedup 1.0000x reference)
_Z13logits_kernelPKDv8_DF16bS1_PKfS3_PDv2_fS5_Pf:
	s_load_dwordx4 s[4:7], s[0:1], 0x0
	s_load_dwordx4 s[12:15], s[0:1], 0x10
	s_load_dwordx4 s[24:27], s[0:1], 0x20
	s_load_dwordx2 s[28:29], s[0:1], 0x30
	s_and_b32 s3, s2, 1
	s_lshl_b32 s3, s3, 3
	s_lshr_b32 s10, s2, 5
	s_or_b32 s10, s10, s3
	s_bfe_u32 s3, s2, 0x20001
	s_lshl_b32 s3, s3, 2
	s_bfe_u32 s8, s2, 0x20003
	s_or_b32 s3, s3, s8
	v_lshrrev_b32_e32 v1, 6, v0
	v_and_b32_e32 v2, 63, v0
	s_movk_i32 s11, 0x3000
	v_lshlrev_b32_e32 v2, 4, v2
	v_and_b32_e32 v5, 31, v0
	v_mad_u32_u24 v2, v1, s11, v2
	v_lshlrev_b32_e32 v5, 2, v5
	s_lshl_b32 s9, s3, 9
	v_add_u32_e32 v3, 0x1000, v2
	v_add_u32_e32 v4, 0x2000, v2
	v_add_u32_e32 v5, s9, v5
	s_mul_i32 s8, s10, 0xc000
	s_mul_i32 s9, s3, 0x30000
	s_waitcnt lgkmcnt(0)
	s_load_dword s22, s[14:15], 0x0
	global_load_dword v248, v5, s[12:13]
	global_load_dword v249, v5, s[12:13] offset:128
	global_load_dword v250, v5, s[12:13] offset:256
	global_load_dword v251, v5, s[12:13] offset:384
	s_add_u32 s4, s4, s8
	s_addc_u32 s5, s5, 0
	s_add_u32 s6, s6, s9
	s_addc_u32 s7, s7, 0
	s_add_u32 s16, s6, 0xc000
	s_addc_u32 s17, s7, 0
	s_add_u32 s18, s6, 0x18000
	s_addc_u32 s19, s7, 0
	s_add_u32 s20, s6, 0x24000
	s_addc_u32 s21, s7, 0
	global_load_dwordx4 v[8:11], v2, s[4:5]
	global_load_dwordx4 v[56:59], v2, s[6:7]
	global_load_dwordx4 v[104:107], v2, s[16:17]
	global_load_dwordx4 v[152:155], v2, s[18:19]
	global_load_dwordx4 v[200:203], v2, s[20:21]
	global_load_dwordx4 v[12:15], v2, s[4:5] offset:1024
	global_load_dwordx4 v[60:63], v2, s[6:7] offset:1024
	global_load_dwordx4 v[108:111], v2, s[16:17] offset:1024
	global_load_dwordx4 v[156:159], v2, s[18:19] offset:1024
	global_load_dwordx4 v[204:207], v2, s[20:21] offset:1024
	global_load_dwordx4 v[16:19], v2, s[4:5] offset:2048
	global_load_dwordx4 v[64:67], v2, s[6:7] offset:2048
	global_load_dwordx4 v[112:115], v2, s[16:17] offset:2048
	global_load_dwordx4 v[160:163], v2, s[18:19] offset:2048
	global_load_dwordx4 v[208:211], v2, s[20:21] offset:2048
	global_load_dwordx4 v[20:23], v2, s[4:5] offset:3072
	global_load_dwordx4 v[68:71], v2, s[6:7] offset:3072
	global_load_dwordx4 v[116:119], v2, s[16:17] offset:3072
	global_load_dwordx4 v[164:167], v2, s[18:19] offset:3072
	global_load_dwordx4 v[212:215], v2, s[20:21] offset:3072
	global_load_dwordx4 v[24:27], v3, s[4:5]
	global_load_dwordx4 v[72:75], v3, s[6:7]
	global_load_dwordx4 v[120:123], v3, s[16:17]
	global_load_dwordx4 v[168:171], v3, s[18:19]
	global_load_dwordx4 v[216:219], v3, s[20:21]
	global_load_dwordx4 v[28:31], v3, s[4:5] offset:1024
	global_load_dwordx4 v[76:79], v3, s[6:7] offset:1024
	global_load_dwordx4 v[124:127], v3, s[16:17] offset:1024
	global_load_dwordx4 v[172:175], v3, s[18:19] offset:1024
	global_load_dwordx4 v[220:223], v3, s[20:21] offset:1024
	global_load_dwordx4 v[32:35], v3, s[4:5] offset:2048
	global_load_dwordx4 v[80:83], v3, s[6:7] offset:2048
	global_load_dwordx4 v[128:131], v3, s[16:17] offset:2048
	global_load_dwordx4 v[176:179], v3, s[18:19] offset:2048
	global_load_dwordx4 v[224:227], v3, s[20:21] offset:2048
	global_load_dwordx4 v[36:39], v3, s[4:5] offset:3072
	global_load_dwordx4 v[84:87], v3, s[6:7] offset:3072
	global_load_dwordx4 v[132:135], v3, s[16:17] offset:3072
	global_load_dwordx4 v[180:183], v3, s[18:19] offset:3072
	global_load_dwordx4 v[228:231], v3, s[20:21] offset:3072
	global_load_dwordx4 v[40:43], v4, s[4:5]
	global_load_dwordx4 v[88:91], v4, s[6:7]
	global_load_dwordx4 v[136:139], v4, s[16:17]
	global_load_dwordx4 v[184:187], v4, s[18:19]
	global_load_dwordx4 v[232:235], v4, s[20:21]
	global_load_dwordx4 v[44:47], v4, s[4:5] offset:1024
	global_load_dwordx4 v[92:95], v4, s[6:7] offset:1024
	global_load_dwordx4 v[140:143], v4, s[16:17] offset:1024
	global_load_dwordx4 v[188:191], v4, s[18:19] offset:1024
	global_load_dwordx4 v[236:239], v4, s[20:21] offset:1024
	global_load_dwordx4 v[48:51], v4, s[4:5] offset:2048
	global_load_dwordx4 v[96:99], v4, s[6:7] offset:2048
	global_load_dwordx4 v[144:147], v4, s[16:17] offset:2048
	global_load_dwordx4 v[192:195], v4, s[18:19] offset:2048
	global_load_dwordx4 v[240:243], v4, s[20:21] offset:2048
	global_load_dwordx4 v[52:55], v4, s[4:5] offset:3072
	global_load_dwordx4 v[100:103], v4, s[6:7] offset:3072
	global_load_dwordx4 v[148:151], v4, s[16:17] offset:3072
	global_load_dwordx4 v[196:199], v4, s[18:19] offset:3072
	global_load_dwordx4 v[244:247], v4, s[20:21] offset:3072
	s_waitcnt vmcnt(58)
	v_mfma_f32_32x32x16_bf16 a[0:15], v[8:11], v[56:59], 0
	s_waitcnt vmcnt(57)
	v_mfma_f32_32x32x16_bf16 a[0:15], v[8:11], v[104:107], a[0:15]
	s_waitcnt vmcnt(56)
	v_mfma_f32_32x32x16_bf16 a[0:15], v[8:11], v[152:155], a[0:15]
	s_waitcnt vmcnt(55)
	v_mfma_f32_32x32x16_bf16 a[0:15], v[8:11], v[200:203], a[0:15]
	s_waitcnt vmcnt(53)
	v_mfma_f32_32x32x16_bf16 a[0:15], v[12:15], v[60:63], a[0:15]
	s_waitcnt vmcnt(52)
	v_mfma_f32_32x32x16_bf16 a[0:15], v[12:15], v[108:111], a[0:15]
	s_waitcnt vmcnt(51)
	v_mfma_f32_32x32x16_bf16 a[0:15], v[12:15], v[156:159], a[0:15]
	s_waitcnt vmcnt(50)
	v_mfma_f32_32x32x16_bf16 a[0:15], v[12:15], v[204:207], a[0:15]
	s_waitcnt vmcnt(48)
	v_mfma_f32_32x32x16_bf16 a[0:15], v[16:19], v[64:67], a[0:15]
	s_waitcnt vmcnt(47)
	v_mfma_f32_32x32x16_bf16 a[0:15], v[16:19], v[112:115], a[0:15]
	s_waitcnt vmcnt(46)
	v_mfma_f32_32x32x16_bf16 a[0:15], v[16:19], v[160:163], a[0:15]
	s_waitcnt vmcnt(45)
	v_mfma_f32_32x32x16_bf16 a[0:15], v[16:19], v[208:211], a[0:15]
	s_waitcnt vmcnt(43)
	v_mfma_f32_32x32x16_bf16 a[0:15], v[20:23], v[68:71], a[0:15]
	s_waitcnt vmcnt(42)
	v_mfma_f32_32x32x16_bf16 a[0:15], v[20:23], v[116:119], a[0:15]
	s_waitcnt vmcnt(41)
	v_mfma_f32_32x32x16_bf16 a[0:15], v[20:23], v[164:167], a[0:15]
	s_waitcnt vmcnt(40)
	v_mfma_f32_32x32x16_bf16 a[0:15], v[20:23], v[212:215], a[0:15]
	s_waitcnt vmcnt(38)
	v_mfma_f32_32x32x16_bf16 a[0:15], v[24:27], v[72:75], a[0:15]
	s_waitcnt vmcnt(37)
	v_mfma_f32_32x32x16_bf16 a[0:15], v[24:27], v[120:123], a[0:15]
	s_waitcnt vmcnt(36)
	v_mfma_f32_32x32x16_bf16 a[0:15], v[24:27], v[168:171], a[0:15]
	s_waitcnt vmcnt(35)
	v_mfma_f32_32x32x16_bf16 a[0:15], v[24:27], v[216:219], a[0:15]
	s_waitcnt vmcnt(33)
	v_mfma_f32_32x32x16_bf16 a[0:15], v[28:31], v[76:79], a[0:15]
	s_waitcnt vmcnt(32)
	v_mfma_f32_32x32x16_bf16 a[0:15], v[28:31], v[124:127], a[0:15]
	s_waitcnt vmcnt(31)
	v_mfma_f32_32x32x16_bf16 a[0:15], v[28:31], v[172:175], a[0:15]
	s_waitcnt vmcnt(30)
	v_mfma_f32_32x32x16_bf16 a[0:15], v[28:31], v[220:223], a[0:15]
	s_waitcnt vmcnt(28)
	v_mfma_f32_32x32x16_bf16 a[0:15], v[32:35], v[80:83], a[0:15]
	s_waitcnt vmcnt(27)
	v_mfma_f32_32x32x16_bf16 a[0:15], v[32:35], v[128:131], a[0:15]
	s_waitcnt vmcnt(26)
	v_mfma_f32_32x32x16_bf16 a[0:15], v[32:35], v[176:179], a[0:15]
	s_waitcnt vmcnt(25)
	v_mfma_f32_32x32x16_bf16 a[0:15], v[32:35], v[224:227], a[0:15]
	s_waitcnt vmcnt(23)
	v_mfma_f32_32x32x16_bf16 a[0:15], v[36:39], v[84:87], a[0:15]
	s_waitcnt vmcnt(22)
	v_mfma_f32_32x32x16_bf16 a[0:15], v[36:39], v[132:135], a[0:15]
	s_waitcnt vmcnt(21)
	v_mfma_f32_32x32x16_bf16 a[0:15], v[36:39], v[180:183], a[0:15]
	s_waitcnt vmcnt(20)
	v_mfma_f32_32x32x16_bf16 a[0:15], v[36:39], v[228:231], a[0:15]
	s_waitcnt vmcnt(18)
	v_mfma_f32_32x32x16_bf16 a[0:15], v[40:43], v[88:91], a[0:15]
	s_waitcnt vmcnt(17)
	v_mfma_f32_32x32x16_bf16 a[0:15], v[40:43], v[136:139], a[0:15]
	s_waitcnt vmcnt(16)
	v_mfma_f32_32x32x16_bf16 a[0:15], v[40:43], v[184:187], a[0:15]
	s_waitcnt vmcnt(15)
	v_mfma_f32_32x32x16_bf16 a[0:15], v[40:43], v[232:235], a[0:15]
	s_waitcnt vmcnt(13)
	v_mfma_f32_32x32x16_bf16 a[0:15], v[44:47], v[92:95], a[0:15]
	s_waitcnt vmcnt(12)
	v_mfma_f32_32x32x16_bf16 a[0:15], v[44:47], v[140:143], a[0:15]
	s_waitcnt vmcnt(11)
	v_mfma_f32_32x32x16_bf16 a[0:15], v[44:47], v[188:191], a[0:15]
	s_waitcnt vmcnt(10)
	v_mfma_f32_32x32x16_bf16 a[0:15], v[44:47], v[236:239], a[0:15]
	v_add_f32_e32 v8, 0, v248
	v_add_f32_e32 v8, v8, v249
	v_add_f32_e32 v8, v8, v250
	v_add_f32_e32 v8, v8, v251
	v_mov_b32_e32 v9, 0x3fb8aa3b
	s_waitcnt lgkmcnt(0)
	v_mul_f32_e32 v9, s22, v9
	v_exp_f32_e32 v9, v9
	v_add_f32_e32 v10, 0x2b8cbccc, v8
	v_div_scale_f32 v11, s[8:9], v10, v10, v9
	v_rcp_f32_e32 v12, v11
	v_div_scale_f32 v13, vcc, v9, v10, v9
	v_fma_f32 v14, -v11, v12, 1.0
	v_fmac_f32_e32 v12, v14, v12
	v_mul_f32_e32 v14, v13, v12
	v_fma_f32 v15, -v11, v14, v13
	v_fmac_f32_e32 v14, v15, v12
	v_fma_f32 v11, -v11, v14, v13
	v_div_fmas_f32 v11, v11, v12, v14
	v_div_fixup_f32 v9, v11, v10, v9
	v_lshlrev_b32_e32 v10, 2, v0
	v_add_u32_e32 v10, 0x4000, v10
	v_cmp_gt_u32_e32 vcc, 32, v0
	s_and_saveexec_b64 s[8:9], vcc
	ds_write2_b32 v10, v8, v9 offset0:128 offset1:160
	s_mov_b64 exec, s[8:9]
	s_waitcnt vmcnt(8)
	v_mfma_f32_32x32x16_bf16 a[0:15], v[48:51], v[96:99], a[0:15]
	s_waitcnt vmcnt(7)
	v_mfma_f32_32x32x16_bf16 a[0:15], v[48:51], v[144:147], a[0:15]
	s_waitcnt vmcnt(6)
	v_mfma_f32_32x32x16_bf16 a[0:15], v[48:51], v[192:195], a[0:15]
	s_waitcnt vmcnt(5)
	v_mfma_f32_32x32x16_bf16 a[0:15], v[48:51], v[240:243], a[0:15]
	v_mul_u32_u24_e32 v1, 0x1080, v1
	s_movk_i32 s4, 0x7f
	s_movk_i32 s6, 0x84
	v_cmp_lt_u32_e32 vcc, s4, v0
	v_lshrrev_b32_e32 v11, 3, v0
	v_and_b32_e32 v10, 31, v0
	v_and_b32_e32 v11, 4, v11
	v_mul_u32_u24_e32 v11, 0x84, v11
	v_lshlrev_b32_e32 v9, 2, v10
	v_bfe_u32 v6, v0, 2, 5
	v_and_b32_e32 v7, 3, v0
	v_add3_u32 v1, v1, v11, v9
	v_lshlrev_b32_e32 v8, 3, v7
	s_waitcnt vmcnt(3)
	v_mfma_f32_32x32x16_bf16 a[0:15], v[52:55], v[100:103], a[0:15]
	s_waitcnt vmcnt(2)
	v_mfma_f32_32x32x16_bf16 a[0:15], v[52:55], v[148:151], a[0:15]
	s_waitcnt vmcnt(1)
	v_mfma_f32_32x32x16_bf16 a[0:15], v[52:55], v[196:199], a[0:15]
	s_waitcnt vmcnt(0)
	v_mfma_f32_32x32x16_bf16 a[0:15], v[52:55], v[244:247], a[0:15]
	s_nop 11
	ds_write_b32 v1, a0
	ds_write_b32 v1, a1 offset:132
	ds_write_b32 v1, a2 offset:264
	ds_write_b32 v1, a3 offset:396
	ds_write_b32 v1, a4 offset:1056
	ds_write_b32 v1, a5 offset:1188
	ds_write_b32 v1, a6 offset:1320
	ds_write_b32 v1, a7 offset:1452
	ds_write_b32 v1, a8 offset:2112
	ds_write_b32 v1, a9 offset:2244
	ds_write_b32 v1, a10 offset:2376
	ds_write_b32 v1, a11 offset:2508
	ds_write_b32 v1, a12 offset:3168
	ds_write_b32 v1, a13 offset:3300
	ds_write_b32 v1, a14 offset:3432
	ds_write_b32 v1, a15 offset:3564
	v_bfe_u32 v6, v0, 2, 5
	v_and_b32_e32 v7, 3, v0
	v_lshlrev_b32_e32 v9, 3, v7
	v_readfirstlane_b32 s30, v0
	v_sub_u32_e32 v10, v6, v9
	s_waitcnt lgkmcnt(0)
	s_barrier
	s_cmpk_ge_u32 s30, 0x80
	s_cbranch_scc1 .Llg_k1
	v_mul_u32_u24_e32 v2, 0x84, v6
	v_lshlrev_b32_e32 v8, 5, v7
	v_add_u32_e32 v2, v2, v8
	v_add_u32_e32 v8, 0x4280, v8
	v_add_u32_e32 v3, 0x1080, v2
	v_add_u32_e32 v4, 0x2100, v2
	v_add_u32_e32 v5, 0x3180, v2
	ds_read_b128 v[48:51], v8
	ds_read_b128 v[52:55], v8 offset:16
	ds_read2_b32 v[16:17], v2 offset0:0 offset1:1
	ds_read2_b32 v[18:19], v2 offset0:2 offset1:3
	ds_read2_b32 v[20:21], v2 offset0:4 offset1:5
	ds_read2_b32 v[22:23], v2 offset0:6 offset1:7
	ds_read2_b32 v[24:25], v3 offset0:0 offset1:1
	ds_read2_b32 v[26:27], v3 offset0:2 offset1:3
	ds_read2_b32 v[28:29], v3 offset0:4 offset1:5
	ds_read2_b32 v[30:31], v3 offset0:6 offset1:7
	ds_read2_b32 v[32:33], v4 offset0:0 offset1:1
	ds_read2_b32 v[34:35], v4 offset0:2 offset1:3
	ds_read2_b32 v[36:37], v4 offset0:4 offset1:5
	ds_read2_b32 v[38:39], v4 offset0:6 offset1:7
	s_waitcnt lgkmcnt(4)
	ds_read2_b32 v[40:41], v5 offset0:0 offset1:1
	ds_read2_b32 v[42:43], v5 offset0:2 offset1:3
	ds_read2_b32 v[44:45], v5 offset0:4 offset1:5
	ds_read2_b32 v[46:47], v5 offset0:6 offset1:7
	s_waitcnt lgkmcnt(0)
	s_branch .Llg_join
